# conversion queue limited to waves 0-2 of each workgroup (less memory-system oversubscription)
# speedup vs baseline: 1.0257x; 1.0160x over previous
.LBB0_756:
	s_mov_b64 s[8:9], -1
	s_cmp_gt_u32 s54, 2
	s_cbranch_scc1 .LBB0_755
	v_mov_b32_e32 v2, 0
	s_and_saveexec_b64 s[8:9], s[40:41]
	s_cbranch_execz .LBB0_760
	s_mov_b64 s[12:13], exec
	v_mbcnt_lo_u32_b32 v2, s12, 0
	v_mbcnt_hi_u32_b32 v2, s13, v2
	v_cmp_eq_u32_e32 vcc, 0, v2
	s_and_saveexec_b64 s[10:11], vcc
	s_cbranch_execz .LBB0_759
	s_bcnt1_i32_b64 s12, s[12:13]
	v_mov_b32_e32 v3, s12
	global_atomic_add v3, v99, v3, s[6:7] sc0

.LBB0_882:
	s_mov_b64 s[6:7], -1
	s_cmp_gt_u32 s54, 2
	s_cbranch_scc1 .LBB0_881
	v_mov_b32_e32 v2, 0
	s_and_saveexec_b64 s[6:7], s[40:41]
	s_cbranch_execz .LBB0_886
	s_mov_b64 s[10:11], exec
	v_mbcnt_lo_u32_b32 v2, s10, 0
	v_mbcnt_hi_u32_b32 v2, s11, v2
	v_cmp_eq_u32_e32 vcc, 0, v2
	s_and_saveexec_b64 s[8:9], vcc
	s_cbranch_execz .LBB0_885
	s_bcnt1_i32_b64 s10, s[10:11]
	v_mov_b32_e32 v3, s10
	global_atomic_add v3, v99, v3, s[4:5] sc0
